# baseline (speedup 1.0000x reference)
_Z11edge_kernelPKfPK15HIP_vector_typeIjLj4EES0_S0_S4_PfS5_:
	s_load_dwordx8 s[64:71], s[0:1], 0x0
	s_load_dwordx4 s[72:75], s[0:1], 0x20
	s_load_dwordx2 s[76:77], s[0:1], 0x30
	s_waitcnt lgkmcnt(0)
	s_mov_b64 s[4:5], s[72:73]
	v_lshrrev_b32_e32 v192, 6, v0
	s_and_b32 s14, s2, 1
	s_lshr_b32 s3, s2, 6
	s_and_b32 s3, s3, 0x3fffff8
	v_lshl_or_b32 v1, s14, 2, v192
	v_or_b32_e32 v1, s3, v1
	v_lshlrev_b32_e32 v176, 4, v1
	v_mov_b32_e32 v177, 0
	v_and_b32_e32 v191, 63, v0
	v_lshlrev_b64 v[2:3], 10, v[176:177]
	s_waitcnt lgkmcnt(0)
	v_lshl_add_u64 v[2:3], s[4:5], 0, v[2:3]
	v_lshlrev_b32_e32 v176, 4, v191
	v_lshl_add_u64 v[184:185], v[2:3], 0, v[176:177]
	global_load_dwordx4 v[2:5], v[184:185], off
	s_mov_b64 s[4:5], 0x400
	v_lshl_add_u64 v[6:7], v[184:185], 0, s[4:5]
	global_load_dwordx4 v[170:173], v[6:7], off
	s_mov_b64 s[4:5], 0x800
	v_lshl_add_u64 v[6:7], v[184:185], 0, s[4:5]
	global_load_dwordx4 v[166:169], v[6:7], off
	s_mov_b64 s[4:5], 0xc00
	v_lshl_add_u64 v[6:7], v[184:185], 0, s[4:5]
	global_load_dwordx4 v[162:165], v[6:7], off
	s_mov_b64 s[4:5], 0x1000
	v_lshl_add_u64 v[6:7], v[184:185], 0, s[4:5]
	global_load_dwordx4 v[158:161], v[6:7], off
	s_mov_b64 s[4:5], 0x1400
	v_lshl_add_u64 v[6:7], v[184:185], 0, s[4:5]
	global_load_dwordx4 v[154:157], v[6:7], off
	s_mov_b64 s[4:5], 0x1800
	v_lshl_add_u64 v[6:7], v[184:185], 0, s[4:5]
	global_load_dwordx4 v[150:153], v[6:7], off
	s_mov_b64 s[4:5], 0x1c00
	v_lshl_add_u64 v[6:7], v[184:185], 0, s[4:5]
	global_load_dwordx4 v[146:149], v[6:7], off
	s_mov_b64 s[4:5], 0x2000
	v_lshl_add_u64 v[6:7], v[184:185], 0, s[4:5]
	global_load_dwordx4 v[110:113], v[6:7], off
	s_mov_b64 s[4:5], 0x2400
	v_lshl_add_u64 v[6:7], v[184:185], 0, s[4:5]
	global_load_dwordx4 v[90:93], v[6:7], off
	s_mov_b64 s[4:5], 0x2800
	v_lshl_add_u64 v[6:7], v[184:185], 0, s[4:5]
	global_load_dwordx4 v[86:89], v[6:7], off
	s_mov_b64 s[4:5], 0x2c00
	v_lshl_add_u64 v[6:7], v[184:185], 0, s[4:5]
	global_load_dwordx4 v[82:85], v[6:7], off
	v_cmp_lt_u32_e32 vcc, 63, v0
	s_and_saveexec_b64 s[4:5], vcc
	s_xor_b64 s[4:5], exec, s[4:5]
	s_cbranch_execz .LBB1_10
	s_mov_b64 s[6:7], s[68:69]
	v_cmp_lt_i32_e32 vcc, 1, v192
	s_and_saveexec_b64 s[8:9], vcc
	s_xor_b64 s[8:9], exec, s[8:9]
	s_cbranch_execz .LBB1_5
	v_cmp_eq_u32_e32 vcc, 2, v192
	s_and_saveexec_b64 s[10:11], vcc
	s_cbranch_execz .LBB1_4
	s_mov_b64 s[12:13], src_shared_base
	v_mov_b32_e32 v177, 0
	s_mov_b32 s12, 0xe800
	s_waitcnt lgkmcnt(0)
	v_lshl_add_u64 v[6:7], s[6:7], 0, v[176:177]
	s_mov_b64 s[16:17], 0x400
	s_cmp_lg_u64 s[12:13], 0
	v_lshl_add_u64 v[6:7], v[6:7], 0, s[16:17]
	s_cselect_b32 m0, 0xe800, -1
	s_nop 0
	global_load_lds_dwordx4 v[6:7], off

.LBB1_5:
	s_andn2_saveexec_b64 s[8:9], s[8:9]
	s_cbranch_execz .LBB1_9
	v_cmp_eq_u32_e32 vcc, 1, v192
	s_and_saveexec_b64 s[10:11], vcc
	s_cbranch_execz .LBB1_8
	s_mov_b64 s[20:21], s[72:73]
	v_add_u32_e32 v194, 0x40000, v176
	v_add_u32_e32 v195, 0x41000, v176
	s_waitcnt lgkmcnt(0)
	global_load_dwordx4 v[196:199], v194, s[20:21]
	global_load_dwordx4 v[200:203], v194, s[20:21] offset:1024
	global_load_dwordx4 v[204:207], v194, s[20:21] offset:2048
	global_load_dwordx4 v[208:211], v194, s[20:21] offset:3072
	global_load_dwordx4 v[212:215], v195, s[20:21]
	global_load_dwordx4 v[216:219], v195, s[20:21] offset:1024
	global_load_dwordx4 v[220:223], v195, s[20:21] offset:2048
	global_load_dwordx4 v[224:227], v195, s[20:21] offset:3072

.LBB1_10:
	s_or_saveexec_b64 s[12:13], s[4:5]
	s_mov_b64 s[8:9], s[64:65]
	s_mov_b64 s[10:11], s[66:67]
	s_waitcnt lgkmcnt(0)
	s_mov_b64 s[4:5], s[74:75]
	s_mov_b64 s[6:7], s[76:77]
	s_lshr_b32 s2, s2, 1
	v_lshlrev_b32_e32 v6, 4, v0
	s_xor_b64 exec, exec, s[12:13]
	s_cbranch_execz .LBB1_12
	s_mov_b64 s[0:1], s[70:71]
	s_lshl_b32 s18, s2, 8
	s_mov_b32 s19, 0
	s_lshl_b64 s[18:19], s[18:19], 2
	s_mov_b64 s[16:17], src_shared_base
	s_waitcnt lgkmcnt(0)
	s_add_u32 s0, s0, s18
	s_addc_u32 s1, s1, s19
	s_mov_b32 s16, 0xe000
	s_cmp_lg_u64 s[16:17], 0
	s_cselect_b32 m0, 0xe000, -1
	s_nop 0
	global_load_lds_dwordx4 v6, s[0:1]

	.amdhsa_kernel _Z16node_post_kernelPKfS0_PKtS0_S2_S0_S0_S0_S0_S0_Pf
		.amdhsa_group_segment_fixed_size 12288
		.amdhsa_private_segment_fixed_size 0
		.amdhsa_kernarg_size 88
		.amdhsa_user_sgpr_count 2
		.amdhsa_user_sgpr_dispatch_ptr 0
		.amdhsa_user_sgpr_queue_ptr 0
		.amdhsa_user_sgpr_kernarg_segment_ptr 1
		.amdhsa_user_sgpr_dispatch_id 0
		.amdhsa_user_sgpr_kernarg_preload_length 0
		.amdhsa_user_sgpr_kernarg_preload_offset 0
		.amdhsa_user_sgpr_private_segment_size 0
		.amdhsa_uses_dynamic_stack 0
		.amdhsa_enable_private_segment 0
		.amdhsa_system_sgpr_workgroup_id_x 1
		.amdhsa_system_sgpr_workgroup_id_y 0
		.amdhsa_system_sgpr_workgroup_id_z 0
		.amdhsa_system_sgpr_workgroup_info 0
		.amdhsa_system_vgpr_workitem_id 0
		.amdhsa_next_free_vgpr 256
		.amdhsa_next_free_sgpr 80
		.amdhsa_accum_offset 256
		.amdhsa_reserve_vcc 1
		.amdhsa_float_round_mode_32 0
		.amdhsa_float_round_mode_16_64 0
		.amdhsa_float_denorm_mode_32 3
		.amdhsa_float_denorm_mode_16_64 3
		.amdhsa_dx10_clamp 1
		.amdhsa_ieee_mode 1
		.amdhsa_fp16_overflow 0
		.amdhsa_tg_split 0
		.amdhsa_exception_fp_ieee_invalid_op 0
		.amdhsa_exception_fp_denorm_src 0
		.amdhsa_exception_fp_ieee_div_zero 0
		.amdhsa_exception_fp_ieee_overflow 0
		.amdhsa_exception_fp_ieee_underflow 0
		.amdhsa_exception_fp_ieee_inexact 0
		.amdhsa_exception_int_div_zero 0
	.end_amdhsa_kernel

amdhsa.kernels:
  - .agpr_count:     0
    .args:
      - .actual_access:  read_only
        .address_space:  global
        .offset:         0
        .size:           8
        .value_kind:     global_buffer
      - .actual_access:  read_only
        .address_space:  global
        .offset:         8
        .size:           8
        .value_kind:     global_buffer
      - .actual_access:  read_only
        .address_space:  global
        .offset:         16
        .size:           8
        .value_kind:     global_buffer
      - .actual_access:  read_only
        .address_space:  global
        .offset:         24
        .size:           8
        .value_kind:     global_buffer
      - .actual_access:  read_only
        .address_space:  global
        .offset:         32
        .size:           8
        .value_kind:     global_buffer
      - .actual_access:  read_only
        .address_space:  global
        .offset:         40
        .size:           8
        .value_kind:     global_buffer
      - .actual_access:  read_only
        .address_space:  global
        .offset:         48
        .size:           8
        .value_kind:     global_buffer
      - .actual_access:  read_only
        .address_space:  global
        .offset:         56
        .size:           8
        .value_kind:     global_buffer
      - .actual_access:  read_only
        .address_space:  global
        .offset:         64
        .size:           8
        .value_kind:     global_buffer
      - .actual_access:  read_only
        .address_space:  global
        .offset:         72
        .size:           8
        .value_kind:     global_buffer
      - .actual_access:  read_only
        .address_space:  global
        .offset:         80
        .size:           8
        .value_kind:     global_buffer
      - .actual_access:  write_only
        .address_space:  global
        .offset:         88
        .size:           8
        .value_kind:     global_buffer
      - .actual_access:  write_only
        .address_space:  global
        .offset:         96
        .size:           8
        .value_kind:     global_buffer
      - .actual_access:  read_only
        .address_space:  global
        .offset:         104
        .size:           8
        .value_kind:     global_buffer
      - .actual_access:  read_only
        .address_space:  global
        .offset:         112
        .size:           8
        .value_kind:     global_buffer
      - .actual_access:  read_only
        .address_space:  global
        .offset:         120
        .size:           8
        .value_kind:     global_buffer
      - .actual_access:  read_only
        .address_space:  global
        .offset:         128
        .size:           8
        .value_kind:     global_buffer
      - .actual_access:  read_only
        .address_space:  global
        .offset:         136
        .size:           8
        .value_kind:     global_buffer
      - .actual_access:  read_only
        .address_space:  global
        .offset:         144
        .size:           8
        .value_kind:     global_buffer
      - .actual_access:  write_only
        .address_space:  global
        .offset:         152
        .size:           8
        .value_kind:     global_buffer
      - .actual_access:  write_only
        .address_space:  global
        .offset:         160
        .size:           8
        .value_kind:     global_buffer
      - .actual_access:  write_only
        .address_space:  global
        .offset:         168
        .size:           8
        .value_kind:     global_buffer
      - .actual_access:  read_only
        .address_space:  global
        .offset:         176
        .size:           8
        .value_kind:     global_buffer
      - .actual_access:  read_only
        .address_space:  global
        .offset:         184
        .size:           8
        .value_kind:     global_buffer
      - .actual_access:  read_only
        .address_space:  global
        .offset:         192
        .size:           8
        .value_kind:     global_buffer
      - .actual_access:  write_only
        .address_space:  global
        .offset:         200
        .size:           8
        .value_kind:     global_buffer
    .group_segment_fixed_size: 40960
    .kernarg_segment_align: 8
    .kernarg_segment_size: 208
    .language:       OpenCL C
    .language_version:
      - 2
      - 0
    .max_flat_workgroup_size: 256
    .name:           _Z10pre_kernelPKfS0_S0_S0_S0_S0_S0_S0_S0_S0_S0_PtPfS0_S0_S0_S0_S0_S0_S2_S2_S2_S0_S0_S0_S1_
    .private_segment_fixed_size: 0
    .sgpr_count:     106
    .sgpr_spill_count: 0
    .symbol:         _Z10pre_kernelPKfS0_S0_S0_S0_S0_S0_S0_S0_S0_S0_PtPfS0_S0_S0_S0_S0_S0_S2_S2_S2_S0_S0_S0_S1_.kd
    .uniform_work_group_size: 1
    .uses_dynamic_stack: false
    .vgpr_count:     128
    .vgpr_spill_count: 0
    .wavefront_size: 64
  - .agpr_count:     0
    .args:
      - .actual_access:  read_only
        .address_space:  global
        .offset:         0
        .size:           8
        .value_kind:     global_buffer
      - .address_space:  global
        .offset:         8
        .size:           8
        .value_kind:     global_buffer
      - .address_space:  global
        .offset:         16
        .size:           8
        .value_kind:     global_buffer
      - .address_space:  global
        .offset:         24
        .size:           8
        .value_kind:     global_buffer
      - .address_space:  global
        .offset:         32
        .size:           8
        .value_kind:     global_buffer
      - .actual_access:  write_only
        .address_space:  global
        .offset:         40
        .size:           8
        .value_kind:     global_buffer
      - .actual_access:  write_only
        .address_space:  global
        .offset:         48
        .size:           8
        .value_kind:     global_buffer
    .group_segment_fixed_size: 79872
    .kernarg_segment_align: 8
    .kernarg_segment_size: 56
    .language:       OpenCL C
    .language_version:
      - 2
      - 0
    .max_flat_workgroup_size: 256
    .name:           _Z11edge_kernelPKfPK15HIP_vector_typeIjLj4EES0_S0_S4_PfS5_
    .private_segment_fixed_size: 0
    .sgpr_count:     26
    .sgpr_spill_count: 0
    .symbol:         _Z11edge_kernelPKfPK15HIP_vector_typeIjLj4EES0_S0_S4_PfS5_.kd
    .uniform_work_group_size: 1
    .uses_dynamic_stack: false
    .vgpr_count:     256
    .vgpr_spill_count: 0
    .wavefront_size: 64
  - .agpr_count:     0
    .args:
      - .actual_access:  read_only
        .address_space:  global
        .offset:         0
        .size:           8
        .value_kind:     global_buffer
      - .actual_access:  read_only
        .address_space:  global
        .offset:         8
        .size:           8
        .value_kind:     global_buffer
      - .actual_access:  read_only
        .address_space:  global
        .offset:         16
        .size:           8
        .value_kind:     global_buffer
      - .actual_access:  read_only
        .address_space:  global
        .offset:         24
        .size:           8
        .value_kind:     global_buffer
      - .actual_access:  read_only
        .address_space:  global
        .offset:         32
        .size:           8
        .value_kind:     global_buffer
      - .actual_access:  read_only
        .address_space:  global
        .offset:         40
        .size:           8
        .value_kind:     global_buffer
      - .actual_access:  read_only
        .address_space:  global
        .offset:         48
        .size:           8
        .value_kind:     global_buffer
      - .actual_access:  read_only
        .address_space:  global
        .offset:         56
        .size:           8
        .value_kind:     global_buffer
      - .actual_access:  read_only
        .address_space:  global
        .offset:         64
        .size:           8
        .value_kind:     global_buffer
      - .actual_access:  read_only
        .address_space:  global
        .offset:         72
        .size:           8
        .value_kind:     global_buffer
      - .actual_access:  write_only
        .address_space:  global
        .offset:         80
        .size:           8
        .value_kind:     global_buffer
    .group_segment_fixed_size: 12288
    .kernarg_segment_align: 8
    .kernarg_segment_size: 88
    .language:       OpenCL C
    .language_version:
      - 2
      - 0
    .max_flat_workgroup_size: 512
    .name:           _Z16node_post_kernelPKfS0_PKtS0_S2_S0_S0_S0_S0_S0_Pf
    .private_segment_fixed_size: 0
    .sgpr_count:     86
    .sgpr_spill_count: 0
    .symbol:         _Z16node_post_kernelPKfS0_PKtS0_S2_S0_S0_S0_S0_S0_Pf.kd
    .uniform_work_group_size: 1
    .uses_dynamic_stack: false
    .vgpr_count:     256
    .vgpr_spill_count: 0
    .wavefront_size: 64
